# speedup vs baseline: 1.0098x; 1.0098x over previous
_ZN12_GLOBAL__N_113search_kernelEPKfS1_PhPf:
	s_load_dwordx2 s[8:9], s[0:1], 0x0
	s_load_dwordx2 s[4:5], s[0:1], 0x10
	s_movk_i32 s3, 0x90
	v_readfirstlane_b32 s10, v0
	v_cmp_gt_u32_e32 vcc, s3, v0
	s_and_saveexec_b64 s[6:7], vcc
	v_mov_b32_e32 v2, -1
	v_lshlrev_b32_e32 v1, 3, v0
	v_mov_b32_e32 v3, v2
	ds_write_b64 v1, v[2:3] offset:16384
	s_or_b64 exec, exec, s[6:7]
	s_waitcnt lgkmcnt(0)
	s_add_u32 s6, s4, 0x240000
	s_addc_u32 s7, s5, 0
	s_lshl_b32 s11, s2, 1
	s_and_b32 s14, s11, 14
	s_ashr_i32 s11, s2, 7
	s_lshr_b32 s15, s10, 6
	s_add_i32 s14, s14, s11
	s_bfe_u32 s2, s2, 0x40003
	s_mul_i32 s11, s15, 24
	v_mul_u32_u24_e32 v2, 0x71d, v0
	v_mul_u32_u24_e32 v4, 0x195, v0
	s_min_u32 s18, s11, 0xa5
	s_mul_i32 s11, s14, 3
	s_mul_i32 s12, s2, 9
	s_mov_b32 s13, 0
	v_lshrrev_b32_e32 v3, 16, v2
	s_movk_i32 s19, 0xffdc
	v_lshrrev_b32_e32 v5, 17, v4
	v_mad_i32_i24 v2, v3, s19, v0
	v_mad_i32_i24 v4, v5, -9, v3
	v_add_u32_e32 v3, s11, v5
	v_mov_b64_e32 v[6:7], s[12:13]
	v_mad_i64_i32 v[8:9], s[16:17], v3, s3, v[6:7]
	v_ashrrev_i32_e32 v5, 31, v4
	v_lshl_add_u64 v[4:5], v[8:9], 0, v[4:5]
	s_movk_i32 s13, 0x240
	v_mov_b64_e32 v[8:9], s[8:9]
	v_mad_u64_u32 v[10:11], s[8:9], v4, s13, v[8:9]
	v_min_u32_e32 v4, 0x1cb, v0
	v_or_b32_e32 v4, 0x200, v4
	v_mad_i32_i24 v11, v5, s13, v11
	v_mul_u32_u24_e32 v5, 0x71d, v4
	v_ashrrev_i32_e32 v3, 31, v2
	v_lshrrev_b32_e32 v5, 16, v5
	v_lshl_add_u64 v[2:3], v[2:3], 4, v[10:11]
	v_mad_i32_i24 v10, v5, s19, v4
	v_mul_u32_u24_e32 v4, 0x653, v4
	v_lshrrev_b32_e32 v11, 19, v4
	v_mad_i32_i24 v4, v11, -9, v5
	v_add_u32_e32 v5, s11, v11
	v_mad_i64_i32 v[6:7], s[8:9], v5, s3, v[6:7]
	v_ashrrev_i32_e32 v5, 31, v4
	v_lshl_add_u64 v[4:5], v[6:7], 0, v[4:5]
	v_mad_u64_u32 v[12:13], s[8:9], v4, s13, v[8:9]
	s_mul_i32 s8, s14, 0x90
	s_barrier
	s_load_dwordx2 s[42:43], s[0:1], 0x8
	s_load_dwordx2 s[62:63], s[0:1], 0x0
	v_mov_b32_e32 v244, v2
	v_mov_b32_e32 v245, v3
	global_load_dwordx4 v[6:9], v[2:3], off
	v_mad_i32_i24 v13, v5, s13, v13
	v_ashrrev_i32_e32 v11, 31, v10
	v_lshl_add_u64 v[10:11], v[10:11], 4, v[12:13]
	v_mov_b32_e32 v246, v10
	v_mov_b32_e32 v247, v11
	global_load_dwordx4 v[10:13], v[10:11], off
	v_and_b32_e32 v1, 63, v0
	s_add_i32 s20, s8, s12
	s_lshl_b32 s20, s20, 10
	v_lshl_add_u32 v164, v1, 4, s20
	s_mul_i32 s9, s14, 0xbd
	s_add_i32 s21, s9, s18
	s_lshl_b32 s21, s21, 10
	v_lshl_add_u32 v165, v1, 4, s21
	s_add_u32 s22, s4, 0x1000
	s_addc_u32 s23, s5, 0
	s_add_u32 s24, s4, 0x2000
	s_addc_u32 s25, s5, 0
	s_mov_b32 s26, s6
	s_mov_b32 s27, s7
	s_add_u32 s28, s6, 0x1000
	s_addc_u32 s29, s7, 0
	s_add_u32 s30, s6, 0x2000
	s_addc_u32 s31, s7, 0
	s_add_u32 s32, s6, 0x3000
	s_addc_u32 s33, s7, 0
	s_add_u32 s34, s6, 0x4000
	s_addc_u32 s35, s7, 0
	s_add_u32 s36, s6, 0x5000
	s_addc_u32 s37, s7, 0
	v_bfe_u32 v166, v0, 4, 2
	v_and_b32_e32 v167, 15, v0
	v_lshlrev_b32_e32 v167, 3, v167
	s_mul_i32 s40, s15, 6
	s_mov_b32 s41, 0x7f000000
	global_load_dwordx4 v[112:115], v164, s[4:5]
	global_load_dwordx4 v[16:19], v165, s[26:27] nt
	global_load_dwordx4 v[20:23], v165, s[26:27] offset:1024 nt
	global_load_dwordx4 v[24:27], v165, s[26:27] offset:2048 nt
	global_load_dwordx4 v[28:31], v165, s[26:27] offset:3072 nt
	global_load_dwordx4 v[32:35], v165, s[28:29] nt
	global_load_dwordx4 v[36:39], v165, s[28:29] offset:1024 nt
	global_load_dwordx4 v[40:43], v165, s[28:29] offset:2048 nt
	global_load_dwordx4 v[44:47], v165, s[28:29] offset:3072 nt
	global_load_dwordx4 v[48:51], v165, s[30:31] nt
	global_load_dwordx4 v[52:55], v165, s[30:31] offset:1024 nt
	global_load_dwordx4 v[56:59], v165, s[30:31] offset:2048 nt
	global_load_dwordx4 v[60:63], v165, s[30:31] offset:3072 nt
	global_load_dwordx4 v[64:67], v165, s[32:33] nt
	global_load_dwordx4 v[68:71], v165, s[32:33] offset:1024 nt
	global_load_dwordx4 v[72:75], v165, s[32:33] offset:2048 nt
	global_load_dwordx4 v[76:79], v165, s[32:33] offset:3072 nt
	global_load_dwordx4 v[80:83], v165, s[34:35] nt
	global_load_dwordx4 v[84:87], v165, s[34:35] offset:1024 nt
	global_load_dwordx4 v[88:91], v165, s[34:35] offset:2048 nt
	global_load_dwordx4 v[92:95], v165, s[34:35] offset:3072 nt
	global_load_dwordx4 v[96:99], v165, s[36:37] nt
	global_load_dwordx4 v[100:103], v165, s[36:37] offset:1024 nt
	global_load_dwordx4 v[104:107], v165, s[36:37] offset:2048 nt
	global_load_dwordx4 v[108:111], v165, s[36:37] offset:3072 nt
	global_load_dwordx4 v[116:119], v164, s[4:5] offset:1024
	v_lshlrev_b32_e32 v14, 4, v0
	s_lshr_b32 s50, s15, 1
	s_and_b32 s51, s15, 1
	s_lshl_b32 s51, s51, 3
	s_mov_b32 s48, 0x1010101
	s_mov_b32 s49, 0x1010101
	s_movk_i32 s58, 0x900
	s_movk_i32 s59, 0xb40
	v_and_b32_e32 v168, 7, v0
	v_lshrrev_b32_e32 v177, 3, v1
	v_or_b32_e32 v177, s51, v177
	v_lshlrev_b32_e32 v169, 3, v177
	v_and_b32_e32 v179, 3, v0
	v_lshlrev_b32_e32 v179, 8, v179
	v_lshl_add_u32 v170, v177, 4, v179
	v_add_u32_e32 v170, s20, v170
	v_lshrrev_b32_e32 v179, 2, v168
	v_and_b32_e32 v180, 3, v0
	v_lshl_or_b32 v171, v179, 4, v180
	v_mul_u32_u24_e32 v179, 11, v168
	v_lshrrev_b32_e32 v179, 5, v179
	v_mul_u32_u24_e32 v180, 3, v179
	v_sub_u32_e32 v180, v168, v180
	v_mul_u32_u24_e32 v181, 0x90, v179
	v_add_u32_e32 v181, v181, v180
	v_mul_u32_u24_e32 v172, 0x240, v181
	v_mul_u32_u24_e32 v181, 0x48, v179
	v_add_u32_e32 v181, v181, v180
	v_mul_u32_u24_e32 v173, 0x120, v181
	v_mul_u32_u24_e32 v181, 0x24, v179
	v_add_u32_e32 v181, v181, v180
	v_mul_u32_u24_e32 v174, 0x90, v181
	v_mul_u32_u24_e32 v181, 9, v179
	v_add_u32_e32 v181, v181, v180
	v_mul_u32_u24_e32 v175, 0x240, v181
	v_add_u32_e32 v176, 8, v168
	s_waitcnt lgkmcnt(0)
	s_mul_i32 s60, s14, 0x3cc00
	s_add_u32 s42, s42, s60
	s_addc_u32 s43, s43, 0
	s_mul_i32 s60, s14, 0xf300
	s_add_u32 s44, s4, s60
	s_addc_u32 s45, s5, 0
	s_add_u32 s44, s44, 0x534000
	s_addc_u32 s45, s45, 0
	s_mul_i32 s60, s14, 0x3cc0
	s_add_u32 s46, s4, s60
	s_addc_u32 s47, s5, 0
	s_add_u32 s46, s46, 0x627000
	s_addc_u32 s47, s47, 0
	v_mov_b32_e32 v152, s42
	v_mov_b32_e32 v153, s43
	v_mov_b32_e32 v154, s44
	v_mov_b32_e32 v155, s45
	v_mov_b32_e32 v159, s46
	v_mov_b32_e32 v161, s47
	s_sub_u32 s60, s42, s62
	s_subb_u32 s61, s43, s63
	s_mul_i32 s62, s14, 0x3cc00
	s_sub_u32 s60, s60, s62
	s_subb_u32 s61, s61, 0
	v_lshl_add_u64 v[244:245], v[244:245], 0, s[60:61]
	v_lshl_add_u64 v[246:247], v[246:247], 0, s[60:61]
	s_lshl_b32 s62, s15, 10
	s_add_i32 s62, s62, 0x46e0
	s_mov_b32 m0, s62
	s_mul_i32 s62, s2, 0xf30
	s_add_u32 s60, s44, s62
	s_addc_u32 s61, s45, 0
	v_lshlrev_b32_e32 v240, 4, v0
	v_mov_b32_e32 v241, 0
	v_lshl_add_u64 v[240:241], v[240:241], 0, s[60:61]
	s_mul_i32 s62, s2, 0x3cc
	s_add_u32 s60, s46, s62
	s_addc_u32 s61, s47, 0
	v_lshlrev_b32_e32 v242, 2, v0
	v_mov_b32_e32 v243, 0
	v_lshl_add_u64 v[242:243], v[242:243], 0, s[60:61]
	global_load_lds_dwordx4 v[244:245], off
	global_load_lds_dwordx4 v[246:247], off
	global_load_lds_dwordx4 v[240:241], off
	global_load_lds_dword v[242:243], off
	s_load_dwordx2 s[2:3], s[0:1], 0x18
	s_waitcnt vmcnt(25)
	ds_write_b128 v14, v[6:9]
	ds_write_b128 v14, v[10:13] offset:8192
	v_mfma_f32_16x16x32_f16 v[120:123], v[16:19], v[112:115], 0
	v_mfma_f32_16x16x32_f16 v[124:127], v[20:23], v[112:115], 0
	v_mfma_f32_16x16x32_f16 v[128:131], v[24:27], v[112:115], 0
	v_mfma_f32_16x16x32_f16 v[132:135], v[28:31], v[112:115], 0
	s_waitcnt vmcnt(21)
	v_mfma_f32_16x16x32_f16 v[136:139], v[32:35], v[112:115], 0
	v_mfma_f32_16x16x32_f16 v[140:143], v[36:39], v[112:115], 0
	v_mfma_f32_16x16x32_f16 v[144:147], v[40:43], v[112:115], 0
	v_mfma_f32_16x16x32_f16 v[148:151], v[44:47], v[112:115], 0
	v_min3_i32 v160, v120, v121, s41
	v_min3_i32 v160, v122, v123, v160
	v_min3_i32 v160, v124, v125, v160
	v_min3_i32 v160, v126, v127, v160
	v_min3_i32 v160, v128, v129, v160
	v_min3_i32 v160, v130, v131, v160
	v_min3_i32 v160, v132, v133, v160
	v_min3_i32 v157, v134, v135, v160
	v_mov_b32_e32 v6, 0
	v_mov_b32_e32 v7, 0x900
	v_mov_b32_e32 v8, 0x240
	s_waitcnt vmcnt(17)
	v_mfma_f32_16x16x32_f16 v[120:123], v[48:51], v[112:115], 0
	v_mfma_f32_16x16x32_f16 v[124:127], v[52:55], v[112:115], 0
	v_mov_b32_e32 v158, 0
	v_mfma_f32_16x16x32_f16 v[128:131], v[56:59], v[112:115], 0
	v_mfma_f32_16x16x32_f16 v[132:135], v[60:63], v[112:115], 0
	v_min3_i32 v160, v136, v137, v157
	v_min3_i32 v160, v138, v139, v160
	v_min3_i32 v160, v140, v141, v160
	v_min3_i32 v160, v142, v143, v160
	v_min3_i32 v160, v144, v145, v160
	v_min3_i32 v160, v146, v147, v160
	v_min3_i32 v160, v148, v149, v160
	v_min3_i32 v156, v150, v151, v160
	v_cmp_ge_i32_e32 vcc, v156, v157
	s_waitcnt vmcnt(13)
	v_mfma_f32_16x16x32_f16 v[136:139], v[64:67], v[112:115], 0
	v_mfma_f32_16x16x32_f16 v[140:143], v[68:71], v[112:115], 0
	v_cndmask_b32_e32 v158, 1, v158, vcc
	v_mfma_f32_16x16x32_f16 v[144:147], v[72:75], v[112:115], 0
	v_mfma_f32_16x16x32_f16 v[148:151], v[76:79], v[112:115], 0
	v_min3_i32 v160, v120, v121, v156
	v_min3_i32 v160, v122, v123, v160
	v_min3_i32 v160, v124, v125, v160
	v_min3_i32 v160, v126, v127, v160
	v_min3_i32 v160, v128, v129, v160
	v_min3_i32 v160, v130, v131, v160
	v_min3_i32 v160, v132, v133, v160
	v_min3_i32 v157, v134, v135, v160
	v_cmp_ge_i32_e32 vcc, v157, v156
	s_waitcnt vmcnt(9)
	v_mfma_f32_16x16x32_f16 v[120:123], v[80:83], v[112:115], 0
	v_mfma_f32_16x16x32_f16 v[124:127], v[84:87], v[112:115], 0
	v_cndmask_b32_e32 v158, 2, v158, vcc
	v_mfma_f32_16x16x32_f16 v[128:131], v[88:91], v[112:115], 0
	v_mfma_f32_16x16x32_f16 v[132:135], v[92:95], v[112:115], 0
	v_min3_i32 v160, v136, v137, v157
	v_min3_i32 v160, v138, v139, v160
	v_min3_i32 v160, v140, v141, v160
	v_min3_i32 v160, v142, v143, v160
	v_min3_i32 v160, v144, v145, v160
	v_min3_i32 v160, v146, v147, v160
	v_min3_i32 v160, v148, v149, v160
	v_min3_i32 v156, v150, v151, v160
	v_cmp_ge_i32_e32 vcc, v156, v157
	s_waitcnt vmcnt(5)
	v_mfma_f32_16x16x32_f16 v[136:139], v[96:99], v[112:115], 0
	v_mfma_f32_16x16x32_f16 v[140:143], v[100:103], v[112:115], 0
	v_cndmask_b32_e32 v158, 3, v158, vcc
	v_mfma_f32_16x16x32_f16 v[144:147], v[104:107], v[112:115], 0
	v_mfma_f32_16x16x32_f16 v[148:151], v[108:111], v[112:115], 0
	v_min3_i32 v160, v120, v121, v156
	v_min3_i32 v160, v122, v123, v160
	v_min3_i32 v160, v124, v125, v160
	v_min3_i32 v160, v126, v127, v160
	v_min3_i32 v160, v128, v129, v160
	v_min3_i32 v160, v130, v131, v160
	v_min3_i32 v160, v132, v133, v160
	v_min3_i32 v157, v134, v135, v160
	v_cmp_ge_i32_e32 vcc, v157, v156
	s_waitcnt vmcnt(4)
	global_load_dwordx4 v[112:115], v164, s[4:5] offset:2048
	v_mfma_f32_16x16x32_f16 v[120:123], v[16:19], v[116:119], 0
	v_mfma_f32_16x16x32_f16 v[124:127], v[20:23], v[116:119], 0
	v_cndmask_b32_e32 v158, 4, v158, vcc
	v_mfma_f32_16x16x32_f16 v[128:131], v[24:27], v[116:119], 0
	v_mfma_f32_16x16x32_f16 v[132:135], v[28:31], v[116:119], 0
	v_min3_i32 v160, v136, v137, v157
	v_min3_i32 v160, v138, v139, v160
	v_min3_i32 v160, v140, v141, v160
	v_min3_i32 v160, v142, v143, v160
	v_min3_i32 v160, v144, v145, v160
	v_min3_i32 v160, v146, v147, v160
	v_min3_i32 v160, v148, v149, v160
	v_min3_i32 v156, v150, v151, v160
	v_cmp_ge_i32_e32 vcc, v156, v157
	v_mfma_f32_16x16x32_f16 v[136:139], v[32:35], v[116:119], 0
	v_mfma_f32_16x16x32_f16 v[140:143], v[36:39], v[116:119], 0
	v_cndmask_b32_e32 v158, 5, v158, vcc
	v_add_u32_e32 v162, s40, v158
	v_lshl_or_b32 v162, v162, 2, v166
	v_mov_b32_e32 v163, v156
	ds_min_u64 v167, v[162:163] offset:16384
	v_mfma_f32_16x16x32_f16 v[144:147], v[40:43], v[116:119], 0
	v_mfma_f32_16x16x32_f16 v[148:151], v[44:47], v[116:119], 0
	v_min3_i32 v160, v120, v121, s41
	v_min3_i32 v160, v122, v123, v160
	v_min3_i32 v160, v124, v125, v160
	v_min3_i32 v160, v126, v127, v160
	v_min3_i32 v160, v128, v129, v160
	v_min3_i32 v160, v130, v131, v160
	v_min3_i32 v160, v132, v133, v160
	v_min3_i32 v157, v134, v135, v160
	v_mfma_f32_16x16x32_f16 v[120:123], v[48:51], v[116:119], 0
	v_mfma_f32_16x16x32_f16 v[124:127], v[52:55], v[116:119], 0
	v_mov_b32_e32 v158, 0
	v_mfma_f32_16x16x32_f16 v[128:131], v[56:59], v[116:119], 0
	v_mfma_f32_16x16x32_f16 v[132:135], v[60:63], v[116:119], 0
	v_min3_i32 v160, v136, v137, v157
	v_min3_i32 v160, v138, v139, v160
	v_min3_i32 v160, v140, v141, v160
	v_min3_i32 v160, v142, v143, v160
	v_min3_i32 v160, v144, v145, v160
	v_min3_i32 v160, v146, v147, v160
	v_min3_i32 v160, v148, v149, v160
	v_min3_i32 v156, v150, v151, v160
	v_cmp_ge_i32_e32 vcc, v156, v157
	v_mfma_f32_16x16x32_f16 v[136:139], v[64:67], v[116:119], 0
	v_mfma_f32_16x16x32_f16 v[140:143], v[68:71], v[116:119], 0
	v_cndmask_b32_e32 v158, 1, v158, vcc
	v_mfma_f32_16x16x32_f16 v[144:147], v[72:75], v[116:119], 0
	v_mfma_f32_16x16x32_f16 v[148:151], v[76:79], v[116:119], 0
	v_min3_i32 v160, v120, v121, v156
	v_min3_i32 v160, v122, v123, v160
	v_min3_i32 v160, v124, v125, v160
	v_min3_i32 v160, v126, v127, v160
	v_min3_i32 v160, v128, v129, v160
	v_min3_i32 v160, v130, v131, v160
	v_min3_i32 v160, v132, v133, v160
	v_min3_i32 v157, v134, v135, v160
	v_cmp_ge_i32_e32 vcc, v157, v156
	v_mfma_f32_16x16x32_f16 v[120:123], v[80:83], v[116:119], 0
	v_mfma_f32_16x16x32_f16 v[124:127], v[84:87], v[116:119], 0
	v_cndmask_b32_e32 v158, 2, v158, vcc
	v_mfma_f32_16x16x32_f16 v[128:131], v[88:91], v[116:119], 0
	v_mfma_f32_16x16x32_f16 v[132:135], v[92:95], v[116:119], 0
	v_min3_i32 v160, v136, v137, v157
	v_min3_i32 v160, v138, v139, v160
	v_min3_i32 v160, v140, v141, v160
	v_min3_i32 v160, v142, v143, v160
	v_min3_i32 v160, v144, v145, v160
	v_min3_i32 v160, v146, v147, v160
	v_min3_i32 v160, v148, v149, v160
	v_min3_i32 v156, v150, v151, v160
	v_cmp_ge_i32_e32 vcc, v156, v157
	v_mfma_f32_16x16x32_f16 v[136:139], v[96:99], v[116:119], 0
	v_mfma_f32_16x16x32_f16 v[140:143], v[100:103], v[116:119], 0
	v_cndmask_b32_e32 v158, 3, v158, vcc
	v_mfma_f32_16x16x32_f16 v[144:147], v[104:107], v[116:119], 0
	v_mfma_f32_16x16x32_f16 v[148:151], v[108:111], v[116:119], 0
	v_min3_i32 v160, v120, v121, v156
	v_min3_i32 v160, v122, v123, v160
	v_min3_i32 v160, v124, v125, v160
	v_min3_i32 v160, v126, v127, v160
	v_min3_i32 v160, v128, v129, v160
	v_min3_i32 v160, v130, v131, v160
	v_min3_i32 v160, v132, v133, v160
	v_min3_i32 v157, v134, v135, v160
	v_cmp_ge_i32_e32 vcc, v157, v156
	s_waitcnt vmcnt(0)
	global_load_dwordx4 v[116:119], v164, s[4:5] offset:3072
	v_mfma_f32_16x16x32_f16 v[120:123], v[16:19], v[112:115], 0
	v_mfma_f32_16x16x32_f16 v[124:127], v[20:23], v[112:115], 0
	v_cndmask_b32_e32 v158, 4, v158, vcc
	v_mfma_f32_16x16x32_f16 v[128:131], v[24:27], v[112:115], 0
	v_mfma_f32_16x16x32_f16 v[132:135], v[28:31], v[112:115], 0
	v_min3_i32 v160, v136, v137, v157
	v_min3_i32 v160, v138, v139, v160
	v_min3_i32 v160, v140, v141, v160
	v_min3_i32 v160, v142, v143, v160
	v_min3_i32 v160, v144, v145, v160
	v_min3_i32 v160, v146, v147, v160
	v_min3_i32 v160, v148, v149, v160
	v_min3_i32 v156, v150, v151, v160
	v_cmp_ge_i32_e32 vcc, v156, v157
	v_mfma_f32_16x16x32_f16 v[136:139], v[32:35], v[112:115], 0
	v_mfma_f32_16x16x32_f16 v[140:143], v[36:39], v[112:115], 0
	v_cndmask_b32_e32 v158, 5, v158, vcc
	v_add_u32_e32 v162, s40, v158
	v_lshl_or_b32 v162, v162, 2, v166
	v_mov_b32_e32 v163, v156
	ds_min_u64 v167, v[162:163] offset:16512
	v_mfma_f32_16x16x32_f16 v[144:147], v[40:43], v[112:115], 0
	v_mfma_f32_16x16x32_f16 v[148:151], v[44:47], v[112:115], 0
	v_min3_i32 v160, v120, v121, s41
	v_min3_i32 v160, v122, v123, v160
	v_min3_i32 v160, v124, v125, v160
	v_min3_i32 v160, v126, v127, v160
	v_min3_i32 v160, v128, v129, v160
	v_min3_i32 v160, v130, v131, v160
	v_min3_i32 v160, v132, v133, v160
	v_min3_i32 v157, v134, v135, v160
	v_mfma_f32_16x16x32_f16 v[120:123], v[48:51], v[112:115], 0
	v_mfma_f32_16x16x32_f16 v[124:127], v[52:55], v[112:115], 0
	v_mov_b32_e32 v158, 0
	v_mfma_f32_16x16x32_f16 v[128:131], v[56:59], v[112:115], 0
	v_mfma_f32_16x16x32_f16 v[132:135], v[60:63], v[112:115], 0
	v_min3_i32 v160, v136, v137, v157
	v_min3_i32 v160, v138, v139, v160
	v_min3_i32 v160, v140, v141, v160
	v_min3_i32 v160, v142, v143, v160
	v_min3_i32 v160, v144, v145, v160
	v_min3_i32 v160, v146, v147, v160
	v_min3_i32 v160, v148, v149, v160
	v_min3_i32 v156, v150, v151, v160
	v_cmp_ge_i32_e32 vcc, v156, v157
	v_mfma_f32_16x16x32_f16 v[136:139], v[64:67], v[112:115], 0
	v_mfma_f32_16x16x32_f16 v[140:143], v[68:71], v[112:115], 0
	v_cndmask_b32_e32 v158, 1, v158, vcc
	v_mfma_f32_16x16x32_f16 v[144:147], v[72:75], v[112:115], 0
	v_mfma_f32_16x16x32_f16 v[148:151], v[76:79], v[112:115], 0
	v_min3_i32 v160, v120, v121, v156
	v_min3_i32 v160, v122, v123, v160
	v_min3_i32 v160, v124, v125, v160
	v_min3_i32 v160, v126, v127, v160
	v_min3_i32 v160, v128, v129, v160
	v_min3_i32 v160, v130, v131, v160
	v_min3_i32 v160, v132, v133, v160
	v_min3_i32 v157, v134, v135, v160
	v_cmp_ge_i32_e32 vcc, v157, v156
	v_mfma_f32_16x16x32_f16 v[120:123], v[80:83], v[112:115], 0
	v_mfma_f32_16x16x32_f16 v[124:127], v[84:87], v[112:115], 0
	v_cndmask_b32_e32 v158, 2, v158, vcc
	v_mfma_f32_16x16x32_f16 v[128:131], v[88:91], v[112:115], 0
	v_mfma_f32_16x16x32_f16 v[132:135], v[92:95], v[112:115], 0
	v_min3_i32 v160, v136, v137, v157
	v_min3_i32 v160, v138, v139, v160
	v_min3_i32 v160, v140, v141, v160
	v_min3_i32 v160, v142, v143, v160
	v_min3_i32 v160, v144, v145, v160
	v_min3_i32 v160, v146, v147, v160
	v_min3_i32 v160, v148, v149, v160
	v_min3_i32 v156, v150, v151, v160
	v_cmp_ge_i32_e32 vcc, v156, v157
	v_mfma_f32_16x16x32_f16 v[136:139], v[96:99], v[112:115], 0
	v_mfma_f32_16x16x32_f16 v[140:143], v[100:103], v[112:115], 0
	v_cndmask_b32_e32 v158, 3, v158, vcc
	v_mfma_f32_16x16x32_f16 v[144:147], v[104:107], v[112:115], 0
	v_mfma_f32_16x16x32_f16 v[148:151], v[108:111], v[112:115], 0
	v_min3_i32 v160, v120, v121, v156
	v_min3_i32 v160, v122, v123, v160
	v_min3_i32 v160, v124, v125, v160
	v_min3_i32 v160, v126, v127, v160
	v_min3_i32 v160, v128, v129, v160
	v_min3_i32 v160, v130, v131, v160
	v_min3_i32 v160, v132, v133, v160
	v_min3_i32 v157, v134, v135, v160
	v_cmp_ge_i32_e32 vcc, v157, v156
	s_waitcnt vmcnt(0)
	global_load_dwordx4 v[112:115], v164, s[22:23]
	v_mfma_f32_16x16x32_f16 v[120:123], v[16:19], v[116:119], 0
	v_mfma_f32_16x16x32_f16 v[124:127], v[20:23], v[116:119], 0
	v_cndmask_b32_e32 v158, 4, v158, vcc
	v_mfma_f32_16x16x32_f16 v[128:131], v[24:27], v[116:119], 0
	v_mfma_f32_16x16x32_f16 v[132:135], v[28:31], v[116:119], 0
	v_min3_i32 v160, v136, v137, v157
	v_min3_i32 v160, v138, v139, v160
	v_min3_i32 v160, v140, v141, v160
	v_min3_i32 v160, v142, v143, v160
	v_min3_i32 v160, v144, v145, v160
	v_min3_i32 v160, v146, v147, v160
	v_min3_i32 v160, v148, v149, v160
	v_min3_i32 v156, v150, v151, v160
	v_cmp_ge_i32_e32 vcc, v156, v157
	v_mfma_f32_16x16x32_f16 v[136:139], v[32:35], v[116:119], 0
	v_mfma_f32_16x16x32_f16 v[140:143], v[36:39], v[116:119], 0
	v_cndmask_b32_e32 v158, 5, v158, vcc
	v_add_u32_e32 v162, s40, v158
	v_lshl_or_b32 v162, v162, 2, v166
	v_mov_b32_e32 v163, v156
	ds_min_u64 v167, v[162:163] offset:16640
	v_mfma_f32_16x16x32_f16 v[144:147], v[40:43], v[116:119], 0
	v_mfma_f32_16x16x32_f16 v[148:151], v[44:47], v[116:119], 0
	v_min3_i32 v160, v120, v121, s41
	v_min3_i32 v160, v122, v123, v160
	v_min3_i32 v160, v124, v125, v160
	v_min3_i32 v160, v126, v127, v160
	v_min3_i32 v160, v128, v129, v160
	v_min3_i32 v160, v130, v131, v160
	v_min3_i32 v160, v132, v133, v160
	v_min3_i32 v157, v134, v135, v160
	v_mfma_f32_16x16x32_f16 v[120:123], v[48:51], v[116:119], 0
	v_mfma_f32_16x16x32_f16 v[124:127], v[52:55], v[116:119], 0
	v_mov_b32_e32 v158, 0
	v_mfma_f32_16x16x32_f16 v[128:131], v[56:59], v[116:119], 0
	v_mfma_f32_16x16x32_f16 v[132:135], v[60:63], v[116:119], 0
	v_min3_i32 v160, v136, v137, v157
	v_min3_i32 v160, v138, v139, v160
	v_min3_i32 v160, v140, v141, v160
	v_min3_i32 v160, v142, v143, v160
	v_min3_i32 v160, v144, v145, v160
	v_min3_i32 v160, v146, v147, v160
	v_min3_i32 v160, v148, v149, v160
	v_min3_i32 v156, v150, v151, v160
	v_cmp_ge_i32_e32 vcc, v156, v157
	v_mfma_f32_16x16x32_f16 v[136:139], v[64:67], v[116:119], 0
	v_mfma_f32_16x16x32_f16 v[140:143], v[68:71], v[116:119], 0
	v_cndmask_b32_e32 v158, 1, v158, vcc
	v_mfma_f32_16x16x32_f16 v[144:147], v[72:75], v[116:119], 0
	v_mfma_f32_16x16x32_f16 v[148:151], v[76:79], v[116:119], 0
	v_min3_i32 v160, v120, v121, v156
	v_min3_i32 v160, v122, v123, v160
	v_min3_i32 v160, v124, v125, v160
	v_min3_i32 v160, v126, v127, v160
	v_min3_i32 v160, v128, v129, v160
	v_min3_i32 v160, v130, v131, v160
	v_min3_i32 v160, v132, v133, v160
	v_min3_i32 v157, v134, v135, v160
	v_cmp_ge_i32_e32 vcc, v157, v156
	v_mfma_f32_16x16x32_f16 v[120:123], v[80:83], v[116:119], 0
	v_mfma_f32_16x16x32_f16 v[124:127], v[84:87], v[116:119], 0
	v_cndmask_b32_e32 v158, 2, v158, vcc
	v_mfma_f32_16x16x32_f16 v[128:131], v[88:91], v[116:119], 0
	v_mfma_f32_16x16x32_f16 v[132:135], v[92:95], v[116:119], 0
	v_min3_i32 v160, v136, v137, v157
	v_min3_i32 v160, v138, v139, v160
	v_min3_i32 v160, v140, v141, v160
	v_min3_i32 v160, v142, v143, v160
	v_min3_i32 v160, v144, v145, v160
	v_min3_i32 v160, v146, v147, v160
	v_min3_i32 v160, v148, v149, v160
	v_min3_i32 v156, v150, v151, v160
	v_cmp_ge_i32_e32 vcc, v156, v157
	v_mfma_f32_16x16x32_f16 v[136:139], v[96:99], v[116:119], 0
	v_mfma_f32_16x16x32_f16 v[140:143], v[100:103], v[116:119], 0
	v_cndmask_b32_e32 v158, 3, v158, vcc
	v_mfma_f32_16x16x32_f16 v[144:147], v[104:107], v[116:119], 0
	v_mfma_f32_16x16x32_f16 v[148:151], v[108:111], v[116:119], 0
	v_min3_i32 v160, v120, v121, v156
	v_min3_i32 v160, v122, v123, v160
	v_min3_i32 v160, v124, v125, v160
	v_min3_i32 v160, v126, v127, v160
	v_min3_i32 v160, v128, v129, v160
	v_min3_i32 v160, v130, v131, v160
	v_min3_i32 v160, v132, v133, v160
	v_min3_i32 v157, v134, v135, v160
	v_cmp_ge_i32_e32 vcc, v157, v156
	s_waitcnt vmcnt(0)
	global_load_dwordx4 v[116:119], v164, s[22:23] offset:1024
	v_mfma_f32_16x16x32_f16 v[120:123], v[16:19], v[112:115], 0
	v_mfma_f32_16x16x32_f16 v[124:127], v[20:23], v[112:115], 0
	v_cndmask_b32_e32 v158, 4, v158, vcc
	v_mfma_f32_16x16x32_f16 v[128:131], v[24:27], v[112:115], 0
	v_mfma_f32_16x16x32_f16 v[132:135], v[28:31], v[112:115], 0
	v_min3_i32 v160, v136, v137, v157
	v_min3_i32 v160, v138, v139, v160
	v_min3_i32 v160, v140, v141, v160
	v_min3_i32 v160, v142, v143, v160
	v_min3_i32 v160, v144, v145, v160
	v_min3_i32 v160, v146, v147, v160
	v_min3_i32 v160, v148, v149, v160
	v_min3_i32 v156, v150, v151, v160
	v_cmp_ge_i32_e32 vcc, v156, v157
	v_mfma_f32_16x16x32_f16 v[136:139], v[32:35], v[112:115], 0
	v_mfma_f32_16x16x32_f16 v[140:143], v[36:39], v[112:115], 0
	v_cndmask_b32_e32 v158, 5, v158, vcc
	v_add_u32_e32 v162, s40, v158
	v_lshl_or_b32 v162, v162, 2, v166
	v_mov_b32_e32 v163, v156
	ds_min_u64 v167, v[162:163] offset:16768
	v_mfma_f32_16x16x32_f16 v[144:147], v[40:43], v[112:115], 0
	v_mfma_f32_16x16x32_f16 v[148:151], v[44:47], v[112:115], 0
	v_min3_i32 v160, v120, v121, s41
	v_min3_i32 v160, v122, v123, v160
	v_min3_i32 v160, v124, v125, v160
	v_min3_i32 v160, v126, v127, v160
	v_min3_i32 v160, v128, v129, v160
	v_min3_i32 v160, v130, v131, v160
	v_min3_i32 v160, v132, v133, v160
	v_min3_i32 v157, v134, v135, v160
	v_mfma_f32_16x16x32_f16 v[120:123], v[48:51], v[112:115], 0
	v_mfma_f32_16x16x32_f16 v[124:127], v[52:55], v[112:115], 0
	v_mov_b32_e32 v158, 0
	v_mfma_f32_16x16x32_f16 v[128:131], v[56:59], v[112:115], 0
	v_mfma_f32_16x16x32_f16 v[132:135], v[60:63], v[112:115], 0
	v_min3_i32 v160, v136, v137, v157
	v_min3_i32 v160, v138, v139, v160
	v_min3_i32 v160, v140, v141, v160
	v_min3_i32 v160, v142, v143, v160
	v_min3_i32 v160, v144, v145, v160
	v_min3_i32 v160, v146, v147, v160
	v_min3_i32 v160, v148, v149, v160
	v_min3_i32 v156, v150, v151, v160
	v_cmp_ge_i32_e32 vcc, v156, v157
	v_mfma_f32_16x16x32_f16 v[136:139], v[64:67], v[112:115], 0
	v_mfma_f32_16x16x32_f16 v[140:143], v[68:71], v[112:115], 0
	v_cndmask_b32_e32 v158, 1, v158, vcc
	v_mfma_f32_16x16x32_f16 v[144:147], v[72:75], v[112:115], 0
	v_mfma_f32_16x16x32_f16 v[148:151], v[76:79], v[112:115], 0
	v_min3_i32 v160, v120, v121, v156
	v_min3_i32 v160, v122, v123, v160
	v_min3_i32 v160, v124, v125, v160
	v_min3_i32 v160, v126, v127, v160
	v_min3_i32 v160, v128, v129, v160
	v_min3_i32 v160, v130, v131, v160
	v_min3_i32 v160, v132, v133, v160
	v_min3_i32 v157, v134, v135, v160
	v_cmp_ge_i32_e32 vcc, v157, v156
	v_mfma_f32_16x16x32_f16 v[120:123], v[80:83], v[112:115], 0
	v_mfma_f32_16x16x32_f16 v[124:127], v[84:87], v[112:115], 0
	v_cndmask_b32_e32 v158, 2, v158, vcc
	v_mfma_f32_16x16x32_f16 v[128:131], v[88:91], v[112:115], 0
	v_mfma_f32_16x16x32_f16 v[132:135], v[92:95], v[112:115], 0
	v_min3_i32 v160, v136, v137, v157
	v_min3_i32 v160, v138, v139, v160
	v_min3_i32 v160, v140, v141, v160
	v_min3_i32 v160, v142, v143, v160
	v_min3_i32 v160, v144, v145, v160
	v_min3_i32 v160, v146, v147, v160
	v_min3_i32 v160, v148, v149, v160
	v_min3_i32 v156, v150, v151, v160
	v_cmp_ge_i32_e32 vcc, v156, v157
	v_mfma_f32_16x16x32_f16 v[136:139], v[96:99], v[112:115], 0
	v_mfma_f32_16x16x32_f16 v[140:143], v[100:103], v[112:115], 0
	v_cndmask_b32_e32 v158, 3, v158, vcc
	v_mfma_f32_16x16x32_f16 v[144:147], v[104:107], v[112:115], 0
	v_mfma_f32_16x16x32_f16 v[148:151], v[108:111], v[112:115], 0
	v_min3_i32 v160, v120, v121, v156
	v_min3_i32 v160, v122, v123, v160
	v_min3_i32 v160, v124, v125, v160
	v_min3_i32 v160, v126, v127, v160
	v_min3_i32 v160, v128, v129, v160
	v_min3_i32 v160, v130, v131, v160
	v_min3_i32 v160, v132, v133, v160
	v_min3_i32 v157, v134, v135, v160
	v_cmp_ge_i32_e32 vcc, v157, v156
	s_waitcnt vmcnt(0)
	global_load_dwordx4 v[112:115], v164, s[22:23] offset:2048
	v_mfma_f32_16x16x32_f16 v[120:123], v[16:19], v[116:119], 0
	v_mfma_f32_16x16x32_f16 v[124:127], v[20:23], v[116:119], 0
	v_cndmask_b32_e32 v158, 4, v158, vcc
	v_mfma_f32_16x16x32_f16 v[128:131], v[24:27], v[116:119], 0
	v_mfma_f32_16x16x32_f16 v[132:135], v[28:31], v[116:119], 0
	v_min3_i32 v160, v136, v137, v157
	v_min3_i32 v160, v138, v139, v160
	v_min3_i32 v160, v140, v141, v160
	v_min3_i32 v160, v142, v143, v160
	v_min3_i32 v160, v144, v145, v160
	v_min3_i32 v160, v146, v147, v160
	v_min3_i32 v160, v148, v149, v160
	v_min3_i32 v156, v150, v151, v160
	v_cmp_ge_i32_e32 vcc, v156, v157
	v_mfma_f32_16x16x32_f16 v[136:139], v[32:35], v[116:119], 0
	v_mfma_f32_16x16x32_f16 v[140:143], v[36:39], v[116:119], 0
	v_cndmask_b32_e32 v158, 5, v158, vcc
	v_add_u32_e32 v162, s40, v158
	v_lshl_or_b32 v162, v162, 2, v166
	v_mov_b32_e32 v163, v156
	ds_min_u64 v167, v[162:163] offset:16896
	v_mfma_f32_16x16x32_f16 v[144:147], v[40:43], v[116:119], 0
	v_mfma_f32_16x16x32_f16 v[148:151], v[44:47], v[116:119], 0
	v_min3_i32 v160, v120, v121, s41
	v_min3_i32 v160, v122, v123, v160
	v_min3_i32 v160, v124, v125, v160
	v_min3_i32 v160, v126, v127, v160
	v_min3_i32 v160, v128, v129, v160
	v_min3_i32 v160, v130, v131, v160
	v_min3_i32 v160, v132, v133, v160
	v_min3_i32 v157, v134, v135, v160
	v_mfma_f32_16x16x32_f16 v[120:123], v[48:51], v[116:119], 0
	v_mfma_f32_16x16x32_f16 v[124:127], v[52:55], v[116:119], 0
	v_mov_b32_e32 v158, 0
	v_mfma_f32_16x16x32_f16 v[128:131], v[56:59], v[116:119], 0
	v_mfma_f32_16x16x32_f16 v[132:135], v[60:63], v[116:119], 0
	v_min3_i32 v160, v136, v137, v157
	v_min3_i32 v160, v138, v139, v160
	v_min3_i32 v160, v140, v141, v160
	v_min3_i32 v160, v142, v143, v160
	v_min3_i32 v160, v144, v145, v160
	v_min3_i32 v160, v146, v147, v160
	v_min3_i32 v160, v148, v149, v160
	v_min3_i32 v156, v150, v151, v160
	v_cmp_ge_i32_e32 vcc, v156, v157
	v_mfma_f32_16x16x32_f16 v[136:139], v[64:67], v[116:119], 0
	v_mfma_f32_16x16x32_f16 v[140:143], v[68:71], v[116:119], 0
	v_cndmask_b32_e32 v158, 1, v158, vcc
	v_mfma_f32_16x16x32_f16 v[144:147], v[72:75], v[116:119], 0
	v_mfma_f32_16x16x32_f16 v[148:151], v[76:79], v[116:119], 0
	v_min3_i32 v160, v120, v121, v156
	v_min3_i32 v160, v122, v123, v160
	v_min3_i32 v160, v124, v125, v160
	v_min3_i32 v160, v126, v127, v160
	v_min3_i32 v160, v128, v129, v160
	v_min3_i32 v160, v130, v131, v160
	v_min3_i32 v160, v132, v133, v160
	v_min3_i32 v157, v134, v135, v160
	v_cmp_ge_i32_e32 vcc, v157, v156
	v_mfma_f32_16x16x32_f16 v[120:123], v[80:83], v[116:119], 0
	v_mfma_f32_16x16x32_f16 v[124:127], v[84:87], v[116:119], 0
	v_cndmask_b32_e32 v158, 2, v158, vcc
	v_mfma_f32_16x16x32_f16 v[128:131], v[88:91], v[116:119], 0
	v_mfma_f32_16x16x32_f16 v[132:135], v[92:95], v[116:119], 0
	v_min3_i32 v160, v136, v137, v157
	v_min3_i32 v160, v138, v139, v160
	v_min3_i32 v160, v140, v141, v160
	v_min3_i32 v160, v142, v143, v160
	v_min3_i32 v160, v144, v145, v160
	v_min3_i32 v160, v146, v147, v160
	v_min3_i32 v160, v148, v149, v160
	v_min3_i32 v156, v150, v151, v160
	v_cmp_ge_i32_e32 vcc, v156, v157
	v_mfma_f32_16x16x32_f16 v[136:139], v[96:99], v[116:119], 0
	v_mfma_f32_16x16x32_f16 v[140:143], v[100:103], v[116:119], 0
	v_cndmask_b32_e32 v158, 3, v158, vcc
	v_mfma_f32_16x16x32_f16 v[144:147], v[104:107], v[116:119], 0
	v_mfma_f32_16x16x32_f16 v[148:151], v[108:111], v[116:119], 0
	v_min3_i32 v160, v120, v121, v156
	v_min3_i32 v160, v122, v123, v160
	v_min3_i32 v160, v124, v125, v160
	v_min3_i32 v160, v126, v127, v160
	v_min3_i32 v160, v128, v129, v160
	v_min3_i32 v160, v130, v131, v160
	v_min3_i32 v160, v132, v133, v160
	v_min3_i32 v157, v134, v135, v160
	v_cmp_ge_i32_e32 vcc, v157, v156
	s_waitcnt vmcnt(0)
	global_load_dwordx4 v[116:119], v164, s[22:23] offset:3072
	v_mfma_f32_16x16x32_f16 v[120:123], v[16:19], v[112:115], 0
	v_mfma_f32_16x16x32_f16 v[124:127], v[20:23], v[112:115], 0
	v_cndmask_b32_e32 v158, 4, v158, vcc
	v_mfma_f32_16x16x32_f16 v[128:131], v[24:27], v[112:115], 0
	v_mfma_f32_16x16x32_f16 v[132:135], v[28:31], v[112:115], 0
	v_min3_i32 v160, v136, v137, v157
	v_min3_i32 v160, v138, v139, v160
	v_min3_i32 v160, v140, v141, v160
	v_min3_i32 v160, v142, v143, v160
	v_min3_i32 v160, v144, v145, v160
	v_min3_i32 v160, v146, v147, v160
	v_min3_i32 v160, v148, v149, v160
	v_min3_i32 v156, v150, v151, v160
	v_cmp_ge_i32_e32 vcc, v156, v157
	v_mfma_f32_16x16x32_f16 v[136:139], v[32:35], v[112:115], 0
	v_mfma_f32_16x16x32_f16 v[140:143], v[36:39], v[112:115], 0
	v_cndmask_b32_e32 v158, 5, v158, vcc
	v_add_u32_e32 v162, s40, v158
	v_lshl_or_b32 v162, v162, 2, v166
	v_mov_b32_e32 v163, v156
	ds_min_u64 v167, v[162:163] offset:17024
	v_mfma_f32_16x16x32_f16 v[144:147], v[40:43], v[112:115], 0
	v_mfma_f32_16x16x32_f16 v[148:151], v[44:47], v[112:115], 0
	v_min3_i32 v160, v120, v121, s41
	v_min3_i32 v160, v122, v123, v160
	v_min3_i32 v160, v124, v125, v160
	v_min3_i32 v160, v126, v127, v160
	v_min3_i32 v160, v128, v129, v160
	v_min3_i32 v160, v130, v131, v160
	v_min3_i32 v160, v132, v133, v160
	v_min3_i32 v157, v134, v135, v160
	s_waitcnt lgkmcnt(0)
	s_barrier
	s_lshl_b32 s60, s50, 7
	v_add_u32_e32 v2, s60, v169
	ds_read_b32 v178, v2 offset:16384
	s_lshl_b32 s60, s50, 10
	v_add_u32_e32 v210, s60, v170
	s_cmp_lt_u32 s50, 2
	s_cbranch_scc0 .Lp1a_y
	s_add_i32 s65, s50, 4
	s_lshl_b32 s60, s65, 7
	v_add_u32_e32 v2, s60, v169
	ds_read_b32 v216, v2 offset:16384
	s_lshl_b32 s60, s65, 10
	v_add_u32_e32 v248, s60, v170
.Lp1a_y:
	v_mfma_f32_16x16x32_f16 v[120:123], v[48:51], v[112:115], 0
	v_mfma_f32_16x16x32_f16 v[124:127], v[52:55], v[112:115], 0
	v_mov_b32_e32 v158, 0
	v_mfma_f32_16x16x32_f16 v[128:131], v[56:59], v[112:115], 0
	v_mfma_f32_16x16x32_f16 v[132:135], v[60:63], v[112:115], 0
	v_min3_i32 v160, v136, v137, v157
	v_min3_i32 v160, v138, v139, v160
	v_min3_i32 v160, v140, v141, v160
	v_min3_i32 v160, v142, v143, v160
	v_min3_i32 v160, v144, v145, v160
	v_min3_i32 v160, v146, v147, v160
	v_min3_i32 v160, v148, v149, v160
	v_min3_i32 v156, v150, v151, v160
	v_cmp_ge_i32_e32 vcc, v156, v157
	s_waitcnt lgkmcnt(0)
	v_lshrrev_b32_e32 v2, 2, v178
	v_mul_u32_u24_e32 v3, 43, v2
	v_lshrrev_b32_e32 v3, 8, v3
	v_mul_u32_u24_e32 v4, 6, v3
	v_sub_u32_e32 v4, v2, v4
	v_mul_u32_u24_e32 v3, 24, v3
	v_min_u32_e32 v3, 0xa5, v3
	v_lshl_add_u32 v3, v4, 2, v3
	v_lshrrev_b32_e32 v4, 2, v168
	v_add_u32_e32 v3, v3, v4
	v_and_b32_e32 v4, 3, v178
	v_lshlrev_b32_e32 v4, 2, v4
	v_and_b32_e32 v5, 3, v168
	v_or_b32_e32 v4, v4, v5
	v_lshl_or_b32 v214, v3, 4, v4
	v_add_u32_e32 v3, s9, v3
	v_lshlrev_b32_e32 v4, 4, v4
	v_lshl_or_b32 v206, v3, 10, v4
	global_load_dwordx4 v[178:181], v206, s[6:7]
	global_load_dwordx4 v[182:185], v206, s[6:7] offset:256
	global_load_dwordx4 v[186:189], v206, s[6:7] offset:512
	global_load_dwordx4 v[190:193], v206, s[6:7] offset:768
	global_load_dwordx4 v[194:197], v206, s[6:7] offset:2048
	global_load_dwordx4 v[198:201], v206, s[6:7] offset:2304
	global_load_dwordx4 v[202:205], v206, s[6:7] offset:2560
	global_load_dwordx4 v[206:209], v206, s[6:7] offset:2816
	global_load_dwordx4 v[210:213], v210, s[4:5]
	s_cmp_lt_u32 s50, 2
	s_cbranch_scc0 .Lp1b_y
	v_lshrrev_b32_e32 v2, 2, v216
	v_mul_u32_u24_e32 v3, 43, v2
	v_lshrrev_b32_e32 v3, 8, v3
	v_mul_u32_u24_e32 v4, 6, v3
	v_sub_u32_e32 v4, v2, v4
	v_mul_u32_u24_e32 v3, 24, v3
	v_min_u32_e32 v3, 0xa5, v3
	v_lshl_add_u32 v3, v4, 2, v3
	v_lshrrev_b32_e32 v4, 2, v168
	v_add_u32_e32 v3, v3, v4
	v_and_b32_e32 v4, 3, v216
	v_lshlrev_b32_e32 v4, 2, v4
	v_and_b32_e32 v5, 3, v168
	v_or_b32_e32 v4, v4, v5
	v_lshl_or_b32 v252, v3, 4, v4
	v_add_u32_e32 v3, s9, v3
	v_lshlrev_b32_e32 v4, 4, v4
	v_lshl_or_b32 v244, v3, 10, v4
	global_load_dwordx4 v[216:219], v244, s[6:7]
	global_load_dwordx4 v[220:223], v244, s[6:7] offset:256
	global_load_dwordx4 v[224:227], v244, s[6:7] offset:512
	global_load_dwordx4 v[228:231], v244, s[6:7] offset:768
	global_load_dwordx4 v[232:235], v244, s[6:7] offset:2048
	global_load_dwordx4 v[236:239], v244, s[6:7] offset:2304
	global_load_dwordx4 v[240:243], v244, s[6:7] offset:2560
	global_load_dwordx4 v[244:247], v244, s[6:7] offset:2816
	global_load_dwordx4 v[248:251], v248, s[4:5]
.Lp1b_y:
	v_mfma_f32_16x16x32_f16 v[136:139], v[64:67], v[112:115], 0
	v_mfma_f32_16x16x32_f16 v[140:143], v[68:71], v[112:115], 0
	v_cndmask_b32_e32 v158, 1, v158, vcc
	v_mfma_f32_16x16x32_f16 v[144:147], v[72:75], v[112:115], 0
	v_mfma_f32_16x16x32_f16 v[148:151], v[76:79], v[112:115], 0
	v_min3_i32 v160, v120, v121, v156
	v_min3_i32 v160, v122, v123, v160
	v_min3_i32 v160, v124, v125, v160
	v_min3_i32 v160, v126, v127, v160
	v_min3_i32 v160, v128, v129, v160
	v_min3_i32 v160, v130, v131, v160
	v_min3_i32 v160, v132, v133, v160
	v_min3_i32 v157, v134, v135, v160
	v_cmp_ge_i32_e32 vcc, v157, v156
	v_mfma_f32_16x16x32_f16 v[120:123], v[80:83], v[112:115], 0
	v_mfma_f32_16x16x32_f16 v[124:127], v[84:87], v[112:115], 0
	v_cndmask_b32_e32 v158, 2, v158, vcc
	v_mfma_f32_16x16x32_f16 v[128:131], v[88:91], v[112:115], 0
	v_mfma_f32_16x16x32_f16 v[132:135], v[92:95], v[112:115], 0
	v_min3_i32 v160, v136, v137, v157
	v_min3_i32 v160, v138, v139, v160
	v_min3_i32 v160, v140, v141, v160
	v_min3_i32 v160, v142, v143, v160
	v_min3_i32 v160, v144, v145, v160
	v_min3_i32 v160, v146, v147, v160
	v_min3_i32 v160, v148, v149, v160
	v_min3_i32 v156, v150, v151, v160
	v_cmp_ge_i32_e32 vcc, v156, v157
	v_mfma_f32_16x16x32_f16 v[136:139], v[96:99], v[112:115], 0
	v_mfma_f32_16x16x32_f16 v[140:143], v[100:103], v[112:115], 0
	v_cndmask_b32_e32 v158, 3, v158, vcc
	v_mfma_f32_16x16x32_f16 v[144:147], v[104:107], v[112:115], 0
	v_mfma_f32_16x16x32_f16 v[148:151], v[108:111], v[112:115], 0
	v_min3_i32 v160, v120, v121, v156
	v_min3_i32 v160, v122, v123, v160
	v_min3_i32 v160, v124, v125, v160
	v_min3_i32 v160, v126, v127, v160
	v_min3_i32 v160, v128, v129, v160
	v_min3_i32 v160, v130, v131, v160
	v_min3_i32 v160, v132, v133, v160
	v_min3_i32 v157, v134, v135, v160
	v_cmp_ge_i32_e32 vcc, v157, v156
	s_cmp_lt_u32 s50, 2
	s_cbranch_scc1 .Lit7a
	s_waitcnt vmcnt(9)
	s_branch .Lit7b
.Lit7a:
	s_waitcnt vmcnt(18)
